# baseline (speedup 1.0000x reference)
_Z11prep_kernelPKfS0_S0_S0_S0_S0_S0_S0_S0_PKiPDv8_DF16bS4_PfS5_S5_PiPt:
	s_cmpk_gt_i32 s2, 0x7f
	s_load_dwordx2 s[4:5], s[0:1], 0x40
	s_load_dwordx4 s[16:19], s[0:1], 0x0
	s_load_dwordx2 s[14:15], s[0:1], 0x10
	s_load_dwordx2 s[20:21], s[0:1], 0x20
	s_load_dwordx4 s[8:11], s[0:1], 0x30
	s_load_dwordx2 s[26:27], s[0:1], 0x48
	s_load_dwordx2 s[28:29], s[0:1], 0x80
	s_cselect_b64 s[6:7], -1, 0
	s_lshl_b32 s12, s2, 4
	s_add_i32 s3, s12, 0xfffff800
	s_cmpk_lt_i32 s2, 0x80
	s_cselect_b32 s22, s12, s3
	s_waitcnt lgkmcnt(0)
	s_cselect_b32 s13, s17, s19
	s_cselect_b32 s16, s16, s18
	s_cselect_b32 s21, s15, s21
	s_cselect_b32 s20, s14, s20
	s_ashr_i32 s23, s22, 31
	s_lshl_b64 s[14:15], s[22:23], 9
	s_add_u32 s14, s16, s14
	s_addc_u32 s15, s13, s15
	s_lshl_b32 s13, s2, 9
	s_and_b32 s13, s13, 0xe00
	s_add_i32 s19, s2, 1
	v_or_b32_e32 v131, s13, v0
	s_lshl_b32 s13, s19, 9
	s_and_b32 s13, s13, 0xe00
	s_add_i32 s18, s2, 2
	v_or_b32_e32 v132, s13, v0
	s_lshl_b32 s13, s18, 9
	s_and_b32 s13, s13, 0xe00
	s_add_i32 s17, s2, 3
	v_or_b32_e32 v133, s13, v0
	s_lshl_b32 s13, s17, 9
	s_and_b32 s13, s13, 0xe00
	s_add_i32 s16, s2, 4
	v_lshlrev_b32_e32 v2, 4, v0
	v_or_b32_e32 v134, s13, v0
	s_lshl_b32 s13, s16, 9
	global_load_dwordx4 v[14:17], v2, s[14:15] nt
	s_and_b32 s13, s13, 0xe00
	s_add_i32 s15, s2, 5
	v_or_b32_e32 v135, s13, v0
	s_lshl_b32 s13, s15, 9
	s_and_b32 s13, s13, 0xe00
	s_add_i32 s14, s2, 6
	v_or_b32_e32 v136, s13, v0
	s_lshl_b32 s13, s14, 9
	s_and_b32 s13, s13, 0xe00
	v_or_b32_e32 v137, s13, v0
	s_add_i32 s13, s2, 7
	v_and_b32_e32 v1, 15, v0
	s_lshl_b32 s22, s13, 9
	v_lshrrev_b32_e32 v128, 6, v0
	s_and_b32 s22, s22, 0xe00
	v_lshl_or_b32 v107, v128, 4, v1
	v_lshlrev_b32_e32 v6, 4, v131
	v_lshlrev_b32_e32 v7, 4, v132
	v_lshlrev_b32_e32 v18, 4, v133
	v_lshlrev_b32_e32 v19, 4, v134
	v_lshlrev_b32_e32 v26, 4, v135
	v_lshlrev_b32_e32 v27, 4, v136
	v_lshlrev_b32_e32 v38, 4, v137
	v_or_b32_e32 v138, s22, v0
	v_lshlrev_b32_e32 v106, 2, v107
	global_load_dwordx4 v[10:13], v6, s[20:21]
	global_load_dwordx4 v[2:5], v7, s[20:21]
	global_load_dwordx4 v[22:25], v18, s[20:21]
	s_nop 0
	global_load_dwordx4 v[6:9], v19, s[20:21]
	global_load_dwordx4 v[30:33], v26, s[20:21]
	s_nop 0
	global_load_dwordx4 v[18:21], v27, s[20:21]
	v_lshlrev_b32_e32 v39, 4, v138
	global_load_dwordx4 v[34:37], v38, s[20:21]
	global_load_dwordx4 v[26:29], v39, s[20:21]
	global_load_dword v129, v106, s[4:5]
	global_load_dword v130, v106, s[10:11]
	v_and_b32_e32 v126, 63, v0
	v_lshlrev_b32_e32 v127, 2, v0
	v_mov_b32_e32 v39, 0
	s_and_b64 vcc, exec, s[6:7]
	v_cmp_gt_u32_e64 s[4:5], 32, v126
	v_lshlrev_b32_e32 v108, 4, v126
	s_cbranch_vccz .LBB0_2
	s_load_dwordx2 s[10:11], s[0:1], 0x28
	s_load_dwordx2 s[20:21], s[0:1], 0x18
	v_mov_b32_e32 v109, v39
	s_waitcnt lgkmcnt(0)
	v_mov_b32_e32 v38, s11
	v_mov_b32_e32 v40, s21
	v_mov_b32_e32 v42, s10
	v_mov_b32_e32 v43, s20
	v_cndmask_b32_e64 v41, v38, v40, s[4:5]
	v_cndmask_b32_e64 v40, v42, v43, s[4:5]
	v_and_b32_e32 v38, 0x7c, v127
	s_lshl_b32 s4, s2, 3
	v_lshlrev_b32_e32 v38, 2, v38
	s_and_b32 s5, s4, 0x78
	v_lshl_add_u64 v[40:41], v[40:41], 0, v[38:39]
	v_or_b32_e32 v38, s5, v128
	s_lshl_b32 s10, s19, 3
	global_load_dwordx4 v[102:105], v[40:41], off
	v_lshl_add_u64 v[40:41], s[8:9], 0, v[108:109]
	v_lshlrev_b32_e32 v38, 10, v38
	s_and_b32 s10, s10, 0x78
	v_lshl_add_u64 v[42:43], v[40:41], 0, v[38:39]
	v_or_b32_e32 v38, s10, v128
	s_lshl_b32 s10, s18, 3
	v_lshlrev_b32_e32 v38, 10, v38
	s_and_b32 s10, s10, 0x78
	v_lshl_add_u64 v[44:45], v[40:41], 0, v[38:39]
	v_or_b32_e32 v38, s10, v128
	s_lshl_b32 s10, s17, 3
	v_lshlrev_b32_e32 v38, 10, v38
	s_and_b32 s10, s10, 0x78
	global_load_dwordx4 v[98:101], v[42:43], off
	global_load_dwordx4 v[66:69], v[44:45], off
	v_lshl_add_u64 v[42:43], v[40:41], 0, v[38:39]
	v_or_b32_e32 v38, s10, v128
	s_lshl_b32 s10, s16, 3
	v_lshlrev_b32_e32 v38, 10, v38
	s_and_b32 s10, s10, 0x78
	v_lshl_add_u64 v[44:45], v[40:41], 0, v[38:39]
	v_or_b32_e32 v38, s10, v128
	s_lshl_b32 s10, s15, 3
	v_lshlrev_b32_e32 v38, 10, v38
	s_and_b32 s10, s10, 0x78
	global_load_dwordx4 v[94:97], v[42:43], off
	global_load_dwordx4 v[62:65], v[44:45], off
	v_lshl_add_u64 v[42:43], v[40:41], 0, v[38:39]
	v_or_b32_e32 v38, s10, v128
	s_lshl_b32 s10, s14, 3
	v_lshlrev_b32_e32 v38, 10, v38
	s_and_b32 s10, s10, 0x78
	v_lshl_add_u64 v[44:45], v[40:41], 0, v[38:39]
	v_or_b32_e32 v38, s10, v128
	s_lshl_b32 s10, s13, 3
	v_lshlrev_b32_e32 v38, 10, v38
	s_and_b32 s10, s10, 0x78
	global_load_dwordx4 v[90:93], v[42:43], off
	global_load_dwordx4 v[58:61], v[44:45], off
	v_lshl_add_u64 v[42:43], v[40:41], 0, v[38:39]
	v_or_b32_e32 v38, s10, v128
	v_lshlrev_b32_e32 v38, 10, v38
	v_lshl_add_u64 v[44:45], v[40:41], 0, v[38:39]
	v_bitop3_b32 v38, s5, v128, 64 bitop3:0xde
	s_add_i32 s5, s4, 0x48
	v_lshlrev_b32_e32 v38, 10, v38
	s_and_b32 s5, s5, 0x78
	global_load_dwordx4 v[86:89], v[42:43], off
	global_load_dwordx4 v[54:57], v[44:45], off
	v_lshl_add_u64 v[42:43], v[40:41], 0, v[38:39]
	v_or_b32_e32 v38, s5, v128
	s_add_i32 s5, s4, 0x50
	v_lshlrev_b32_e32 v38, 10, v38
	s_and_b32 s5, s5, 0x78
	v_lshl_add_u64 v[44:45], v[40:41], 0, v[38:39]
	v_or_b32_e32 v38, s5, v128
	s_add_i32 s5, s4, 0x58
	v_lshlrev_b32_e32 v38, 10, v38
	s_and_b32 s5, s5, 0x78
	global_load_dwordx4 v[82:85], v[42:43], off
	global_load_dwordx4 v[50:53], v[44:45], off
	v_lshl_add_u64 v[42:43], v[40:41], 0, v[38:39]
	v_or_b32_e32 v38, s5, v128
	s_add_i32 s5, s4, 0x60
	v_lshlrev_b32_e32 v38, 10, v38
	s_and_b32 s5, s5, 0x78
	v_lshl_add_u64 v[44:45], v[40:41], 0, v[38:39]
	v_or_b32_e32 v38, s5, v128
	s_add_i32 s5, s4, 0x68
	v_lshlrev_b32_e32 v38, 10, v38
	s_and_b32 s5, s5, 0x78
	v_lshl_add_u64 v[70:71], v[40:41], 0, v[38:39]
	v_or_b32_e32 v38, s5, v128
	s_add_i32 s5, s4, 0x70
	v_lshlrev_b32_e32 v38, 10, v38
	s_and_b32 s5, s5, 0x78
	v_lshl_add_u64 v[72:73], v[40:41], 0, v[38:39]
	v_or_b32_e32 v38, s5, v128
	s_addk_i32 s4, 0x78
	v_lshlrev_b32_e32 v38, 10, v38
	s_and_b32 s4, s4, 0x78
	v_lshl_add_u64 v[110:111], v[40:41], 0, v[38:39]
	v_or_b32_e32 v38, s4, v128
	v_lshlrev_b32_e32 v38, 10, v38
	global_load_dwordx4 v[78:81], v[42:43], off
	global_load_dwordx4 v[46:49], v[44:45], off
	global_load_dwordx4 v[74:77], v[70:71], off
	s_nop 0
	global_load_dwordx4 v[42:45], v[72:73], off
	v_lshl_add_u64 v[112:113], v[40:41], 0, v[38:39]
	global_load_dwordx4 v[70:73], v[110:111], off
	global_load_dwordx4 v[38:41], v[112:113], off
	v_lshl_or_b32 v158, s2, 3, v128
	v_lshlrev_b32_e32 v158, 12, v158
	v_lshl_add_u32 v158, v126, 4, v158
	global_load_dwordx4 v[142:145], v158, s[26:27] nt
	global_load_dwordx4 v[146:149], v158, s[26:27] offset:1024 nt
	global_load_dwordx4 v[150:153], v158, s[26:27] offset:2048 nt
	global_load_dwordx4 v[154:157], v158, s[26:27] offset:3072 nt
	s_mov_b64 s[4:5], 0
	s_andn2_b64 vcc, exec, s[4:5]
	s_cbranch_vccnz .LBB0_4
	s_branch .LBB0_3

.LBB0_3:
	v_and_b32_e32 v38, 0x7c, v127
	v_lshlrev_b32_e32 v66, 2, v38
	v_mov_b32_e32 v67, 0
	v_lshlrev_b32_e32 v38, 5, v131
	v_lshl_add_u64 v[68:69], s[8:9], 0, v[66:67]
	v_and_b32_e32 v66, 0x1fc00, v38
	v_lshlrev_b32_e32 v38, 5, v132
	v_lshl_add_u64 v[46:47], v[68:69], 0, v[66:67]
	v_and_b32_e32 v66, 0x1fc00, v38
	v_lshl_add_u64 v[48:49], v[68:69], 0, v[66:67]
	global_load_dwordx4 v[38:41], v[46:47], off
	global_load_dwordx4 v[42:45], v[48:49], off
	v_lshlrev_b32_e32 v46, 5, v133
	v_and_b32_e32 v66, 0x1fc00, v46
	v_lshlrev_b32_e32 v46, 5, v134
	v_lshl_add_u64 v[54:55], v[68:69], 0, v[66:67]
	v_and_b32_e32 v66, 0x1fc00, v46
	v_lshl_add_u64 v[56:57], v[68:69], 0, v[66:67]
	global_load_dwordx4 v[46:49], v[54:55], off
	global_load_dwordx4 v[50:53], v[56:57], off
	v_lshlrev_b32_e32 v54, 5, v135
	v_and_b32_e32 v66, 0x1fc00, v54
	v_lshlrev_b32_e32 v54, 5, v136
	v_lshl_add_u64 v[62:63], v[68:69], 0, v[66:67]
	v_and_b32_e32 v66, 0x1fc00, v54
	v_lshl_add_u64 v[64:65], v[68:69], 0, v[66:67]
	global_load_dwordx4 v[54:57], v[62:63], off
	global_load_dwordx4 v[58:61], v[64:65], off
	v_lshlrev_b32_e32 v62, 5, v137
	v_and_b32_e32 v66, 0x1fc00, v62
	v_lshl_add_u64 v[62:63], v[68:69], 0, v[66:67]
	v_lshlrev_b32_e32 v66, 5, v138
	v_and_b32_e32 v66, 0x1fc00, v66
	v_lshl_add_u64 v[66:67], v[68:69], 0, v[66:67]
	global_load_dwordx4 v[62:65], v[62:63], off
	s_waitcnt vmcnt(6)
	v_cvt_pk_bf16_f32 v110, v38, v39
	global_load_dwordx4 v[66:69], v[66:67], off
	v_lshl_or_b32 v158, s2, 3, v128
	v_lshlrev_b32_e32 v158, 12, v158
	v_lshl_add_u32 v158, v126, 4, v158
	global_load_dwordx4 v[142:145], v158, s[26:27] nt
	global_load_dwordx4 v[146:149], v158, s[26:27] offset:1024 nt
	global_load_dwordx4 v[150:153], v158, s[26:27] offset:2048 nt
	global_load_dwordx4 v[154:157], v158, s[26:27] offset:3072 nt
	v_cvt_pk_bf16_f32 v111, v40, v41
	s_waitcnt vmcnt(10)
	v_cvt_pk_bf16_f32 v112, v42, v43
	v_cvt_pk_bf16_f32 v113, v44, v45
	s_waitcnt vmcnt(9)
	v_cvt_pk_bf16_f32 v114, v46, v47
	v_cvt_pk_bf16_f32 v115, v48, v49
	s_waitcnt vmcnt(8)
	v_cvt_pk_bf16_f32 v116, v50, v51
	v_cvt_pk_bf16_f32 v117, v52, v53
	s_waitcnt vmcnt(7)
	v_cvt_pk_bf16_f32 v118, v54, v55
	v_cvt_pk_bf16_f32 v119, v56, v57
	s_waitcnt vmcnt(6)
	v_cvt_pk_bf16_f32 v120, v58, v59
	v_cvt_pk_bf16_f32 v121, v60, v61
	s_waitcnt vmcnt(5)
	v_cvt_pk_bf16_f32 v122, v62, v63
	v_cvt_pk_bf16_f32 v123, v64, v65
	s_waitcnt vmcnt(4)
	v_cvt_pk_bf16_f32 v124, v66, v67
	v_cvt_pk_bf16_f32 v125, v68, v69
.LBB0_4:
	s_mov_b64 s[8:9], -1
	s_and_b64 vcc, exec, s[6:7]
	s_cbranch_vccz .LBB0_8
	v_mov_b32_e32 v109, 0x3db504f3
	v_cmp_gt_u32_e32 vcc, 32, v126
	v_lshlrev_b32_e32 v139, 2, v126
	s_mov_b32 s4, 0x11000
	v_cndmask_b32_e32 v140, 1.0, v109, vcc
	s_waitcnt vmcnt(20)
	v_pk_mul_f32 v[104:105], v[140:141], v[104:105] op_sel_hi:[0,1]
	v_pk_mul_f32 v[102:103], v[140:141], v[102:103] op_sel_hi:[0,1]
	v_mul_u32_u24_e32 v109, 0x1040, v128
	v_add3_u32 v109, v109, v139, s4
	s_waitcnt vmcnt(19)
	v_mul_f32_e32 v139, v103, v99
	v_mul_f32_e32 v140, v105, v101
	s_and_b32 s4, s2, 15
	v_fmac_f32_e32 v139, v102, v98
	v_fmac_f32_e32 v140, v104, v100
	s_mulk_i32 s4, 0x104
	v_add_f32_e32 v139, v139, v140
	v_add_u32_e32 v140, s4, v109
	ds_write_b32 v140, v139
	s_waitcnt vmcnt(18)
	v_mul_f32_e32 v139, v103, v67
	v_mul_f32_e32 v140, v105, v69
	s_and_b32 s4, s19, 15
	v_fmac_f32_e32 v139, v102, v66
	v_fmac_f32_e32 v140, v104, v68
	s_mulk_i32 s4, 0x104
	v_add_f32_e32 v139, v139, v140
	v_add_u32_e32 v140, s4, v109
	ds_write_b32 v140, v139
	s_waitcnt vmcnt(17)
	v_mul_f32_e32 v139, v103, v95
	v_mul_f32_e32 v140, v105, v97
	s_and_b32 s4, s18, 15
	v_fmac_f32_e32 v139, v102, v94
	v_fmac_f32_e32 v140, v104, v96
	s_mulk_i32 s4, 0x104
	v_add_f32_e32 v139, v139, v140
	v_add_u32_e32 v140, s4, v109
	ds_write_b32 v140, v139
	s_waitcnt vmcnt(16)
	v_mul_f32_e32 v139, v103, v63
	v_mul_f32_e32 v140, v105, v65
	s_and_b32 s4, s17, 15
	v_fmac_f32_e32 v139, v102, v62
	v_fmac_f32_e32 v140, v104, v64
	s_mulk_i32 s4, 0x104
	v_add_f32_e32 v139, v139, v140
	v_add_u32_e32 v140, s4, v109
	ds_write_b32 v140, v139
	s_waitcnt vmcnt(15)
	v_mul_f32_e32 v139, v103, v91
	v_mul_f32_e32 v140, v105, v93
	s_and_b32 s4, s16, 15
	v_fmac_f32_e32 v139, v102, v90
	v_fmac_f32_e32 v140, v104, v92
	s_mulk_i32 s4, 0x104
	v_add_f32_e32 v139, v139, v140
	v_add_u32_e32 v140, s4, v109
	ds_write_b32 v140, v139
	s_waitcnt vmcnt(14)
	v_mul_f32_e32 v139, v103, v59
	v_mul_f32_e32 v140, v105, v61
	s_and_b32 s4, s15, 15
	v_fmac_f32_e32 v139, v102, v58
	v_fmac_f32_e32 v140, v104, v60
	s_mulk_i32 s4, 0x104
	v_add_f32_e32 v139, v139, v140
	v_add_u32_e32 v140, s4, v109
	ds_write_b32 v140, v139
	s_waitcnt vmcnt(13)
	v_mul_f32_e32 v139, v103, v87
	v_mul_f32_e32 v140, v105, v89
	s_and_b32 s4, s14, 15
	v_fmac_f32_e32 v139, v102, v86
	v_fmac_f32_e32 v140, v104, v88
	s_mulk_i32 s4, 0x104
	v_add_f32_e32 v139, v139, v140
	v_add_u32_e32 v140, s4, v109
	ds_write_b32 v140, v139
	s_waitcnt vmcnt(12)
	v_mul_f32_e32 v139, v103, v55
	v_mul_f32_e32 v140, v105, v57
	s_and_b32 s4, s13, 15
	v_fmac_f32_e32 v139, v102, v54
	v_fmac_f32_e32 v140, v104, v56
	s_mulk_i32 s4, 0x104
	v_add_f32_e32 v139, v139, v140
	v_add_u32_e32 v140, s4, v109
	s_add_i32 s8, s2, 8
	ds_write_b32 v140, v139
	s_waitcnt vmcnt(11)
	v_mul_f32_e32 v139, v103, v83
	v_mul_f32_e32 v140, v105, v85
	s_and_b32 s4, s8, 15
	v_fmac_f32_e32 v139, v102, v82
	v_fmac_f32_e32 v140, v104, v84
	s_mulk_i32 s4, 0x104
	v_add_f32_e32 v139, v139, v140
	v_add_u32_e32 v140, s4, v109
	s_add_i32 s9, s2, 9
	ds_write_b32 v140, v139
	s_waitcnt vmcnt(10)
	v_mul_f32_e32 v139, v103, v51
	v_mul_f32_e32 v140, v105, v53
	s_and_b32 s4, s9, 15
	v_fmac_f32_e32 v139, v102, v50
	v_fmac_f32_e32 v140, v104, v52
	s_mulk_i32 s4, 0x104
	v_add_f32_e32 v139, v139, v140
	v_add_u32_e32 v140, s4, v109
	s_add_i32 s10, s2, 10
	ds_write_b32 v140, v139
	s_waitcnt vmcnt(9)
	v_mul_f32_e32 v139, v103, v79
	v_mul_f32_e32 v140, v105, v81
	s_and_b32 s4, s10, 15
	v_fmac_f32_e32 v139, v102, v78
	v_fmac_f32_e32 v140, v104, v80
	s_mulk_i32 s4, 0x104
	v_add_f32_e32 v139, v139, v140
	v_add_u32_e32 v140, s4, v109
	s_add_i32 s11, s2, 11
	ds_write_b32 v140, v139
	s_waitcnt vmcnt(8)
	v_mul_f32_e32 v139, v103, v47
	v_mul_f32_e32 v140, v105, v49
	s_and_b32 s4, s11, 15
	v_fmac_f32_e32 v139, v102, v46
	v_fmac_f32_e32 v140, v104, v48
	s_mulk_i32 s4, 0x104
	v_add_f32_e32 v139, v139, v140
	v_add_u32_e32 v140, s4, v109
	s_add_i32 s20, s2, 12
	ds_write_b32 v140, v139
	s_waitcnt vmcnt(7)
	v_mul_f32_e32 v139, v103, v75
	v_mul_f32_e32 v140, v105, v77
	s_and_b32 s4, s20, 15
	v_fmac_f32_e32 v139, v102, v74
	v_fmac_f32_e32 v140, v104, v76
	s_mulk_i32 s4, 0x104
	v_add_f32_e32 v139, v139, v140
	v_add_u32_e32 v140, s4, v109
	s_add_i32 s21, s2, 13
	ds_write_b32 v140, v139
	s_waitcnt vmcnt(6)
	v_mul_f32_e32 v139, v103, v43
	v_mul_f32_e32 v140, v105, v45
	s_and_b32 s4, s21, 15
	v_fmac_f32_e32 v139, v102, v42
	v_fmac_f32_e32 v140, v104, v44
	s_mulk_i32 s4, 0x104
	v_add_f32_e32 v139, v139, v140
	v_add_u32_e32 v140, s4, v109
	s_add_i32 s22, s2, 14
	ds_write_b32 v140, v139
	s_waitcnt vmcnt(5)
	v_mul_f32_e32 v139, v103, v71
	v_mul_f32_e32 v140, v105, v73
	s_and_b32 s4, s22, 15
	v_fmac_f32_e32 v139, v102, v70
	v_fmac_f32_e32 v140, v104, v72
	s_mulk_i32 s4, 0x104
	s_waitcnt vmcnt(4)
	v_mul_f32_e32 v103, v103, v39
	s_add_i32 s23, s2, 15
	v_add_f32_e32 v139, v139, v140
	v_add_u32_e32 v140, s4, v109
	v_fmac_f32_e32 v103, v102, v38
	v_mul_f32_e32 v102, v105, v41
	s_and_b32 s4, s23, 15
	v_fmac_f32_e32 v102, v104, v40
	s_mulk_i32 s4, 0x104
	v_add_f32_e32 v102, v103, v102
	v_add_u32_e32 v103, s4, v109
	v_cmp_lt_u32_e32 vcc, 31, v126
	ds_write_b32 v140, v139
	ds_write_b32 v103, v102
	s_and_saveexec_b64 s[4:5], vcc
	s_cbranch_execz .LBB0_7
	v_mul_u32_u24_e32 v102, 0x110, v128
	v_lshlrev_b32_e32 v103, 3, v126
	s_mov_b32 s24, 0x8800
	v_add3_u32 v102, v102, v103, s24
	s_lshl_b32 s24, s2, 3
	s_lshl_b32 s19, s19, 3
	s_and_b32 s24, s24, 0x78
	s_and_b32 s19, s19, 0x78
	s_mulk_i32 s24, 0x110
	s_mulk_i32 s19, 0x110
	s_lshl_b32 s18, s18, 3
	s_lshl_b32 s17, s17, 3
	v_cvt_pk_bf16_f32 v101, v100, v101
	v_cvt_pk_bf16_f32 v100, v98, v99
	v_add_u32_e32 v98, s24, v102
	v_cvt_pk_bf16_f32 v69, v68, v69
	v_cvt_pk_bf16_f32 v68, v66, v67
	v_add_u32_e32 v66, s19, v102
	s_and_b32 s18, s18, 0x78
	s_and_b32 s17, s17, 0x78
	v_add_u32_e32 v98, 0xffffff00, v98
	v_add_u32_e32 v66, 0xffffff00, v66
	s_mulk_i32 s18, 0x110
	s_mulk_i32 s17, 0x110
	s_lshl_b32 s16, s16, 3
	s_lshl_b32 s15, s15, 3
	ds_write_b64 v98, v[100:101]
	ds_write_b64 v66, v[68:69]
	v_add_u32_e32 v68, s18, v102
	v_cvt_pk_bf16_f32 v65, v64, v65
	v_cvt_pk_bf16_f32 v64, v62, v63
	v_add_u32_e32 v62, s17, v102
	s_and_b32 s16, s16, 0x78
	s_and_b32 s15, s15, 0x78
	v_cvt_pk_bf16_f32 v67, v96, v97
	v_cvt_pk_bf16_f32 v66, v94, v95
	v_add_u32_e32 v68, 0xffffff00, v68
	v_add_u32_e32 v62, 0xffffff00, v62
	s_mulk_i32 s16, 0x110
	s_mulk_i32 s15, 0x110
	s_lshl_b32 s14, s14, 3
	s_lshl_b32 s13, s13, 3
	ds_write_b64 v68, v[66:67]
	ds_write_b64 v62, v[64:65]
	v_add_u32_e32 v64, s16, v102
	v_cvt_pk_bf16_f32 v61, v60, v61
	v_cvt_pk_bf16_f32 v60, v58, v59
	v_add_u32_e32 v58, s15, v102
	s_and_b32 s14, s14, 0x78
	s_and_b32 s13, s13, 0x78
	v_cvt_pk_bf16_f32 v63, v92, v93
	v_cvt_pk_bf16_f32 v62, v90, v91
	v_add_u32_e32 v64, 0xffffff00, v64
	v_add_u32_e32 v58, 0xffffff00, v58
	s_mulk_i32 s14, 0x110
	s_mulk_i32 s13, 0x110
	s_lshl_b32 s8, s8, 3
	ds_write_b64 v64, v[62:63]
	ds_write_b64 v58, v[60:61]
	v_add_u32_e32 v60, s14, v102
	v_cvt_pk_bf16_f32 v57, v56, v57
	v_cvt_pk_bf16_f32 v56, v54, v55
	v_add_u32_e32 v54, s13, v102
	s_and_b32 s8, s8, 0x78
	v_cvt_pk_bf16_f32 v59, v88, v89
	v_cvt_pk_bf16_f32 v58, v86, v87
	v_add_u32_e32 v60, 0xffffff00, v60
	v_add_u32_e32 v54, 0xffffff00, v54
	s_mulk_i32 s8, 0x110
	ds_write_b64 v60, v[58:59]
	ds_write_b64 v54, v[56:57]
	v_add_u32_e32 v56, s8, v102
	s_lshl_b32 s8, s9, 3
	s_and_b32 s8, s8, 0x78
	s_mulk_i32 s8, 0x110
	v_cvt_pk_bf16_f32 v53, v52, v53
	v_cvt_pk_bf16_f32 v52, v50, v51
	v_add_u32_e32 v50, s8, v102
	s_lshl_b32 s8, s10, 3
	s_and_b32 s8, s8, 0x78
	v_cvt_pk_bf16_f32 v55, v84, v85
	v_cvt_pk_bf16_f32 v54, v82, v83
	v_add_u32_e32 v56, 0xffffff00, v56
	v_add_u32_e32 v50, 0xffffff00, v50
	s_mulk_i32 s8, 0x110
	ds_write_b64 v56, v[54:55]
	ds_write_b64 v50, v[52:53]
	v_add_u32_e32 v52, s8, v102
	s_lshl_b32 s8, s11, 3
	s_and_b32 s8, s8, 0x78
	s_mulk_i32 s8, 0x110
	v_cvt_pk_bf16_f32 v49, v48, v49
	v_cvt_pk_bf16_f32 v48, v46, v47
	v_add_u32_e32 v46, s8, v102
	s_lshl_b32 s8, s20, 3
	s_and_b32 s8, s8, 0x78
	v_cvt_pk_bf16_f32 v51, v80, v81
	v_cvt_pk_bf16_f32 v50, v78, v79
	v_add_u32_e32 v52, 0xffffff00, v52
	v_add_u32_e32 v46, 0xffffff00, v46
	s_mulk_i32 s8, 0x110
	ds_write_b64 v52, v[50:51]
	ds_write_b64 v46, v[48:49]
	v_add_u32_e32 v48, s8, v102
	s_lshl_b32 s8, s21, 3
	s_and_b32 s8, s8, 0x78
	s_mulk_i32 s8, 0x110
	v_cvt_pk_bf16_f32 v45, v44, v45
	v_cvt_pk_bf16_f32 v44, v42, v43
	v_add_u32_e32 v42, s8, v102
	s_lshl_b32 s8, s22, 3
	s_and_b32 s8, s8, 0x78
	v_cvt_pk_bf16_f32 v47, v76, v77
	v_cvt_pk_bf16_f32 v46, v74, v75
	v_add_u32_e32 v48, 0xffffff00, v48
	v_add_u32_e32 v42, 0xffffff00, v42
	s_mulk_i32 s8, 0x110
	ds_write_b64 v48, v[46:47]
	ds_write_b64 v42, v[44:45]
	v_add_u32_e32 v44, s8, v102
	s_lshl_b32 s8, s23, 3
	s_and_b32 s8, s8, 0x78
	s_mulk_i32 s8, 0x110
	v_cvt_pk_bf16_f32 v41, v40, v41
	v_cvt_pk_bf16_f32 v40, v38, v39
	v_add_u32_e32 v38, s8, v102
	v_cvt_pk_bf16_f32 v43, v72, v73
	v_cvt_pk_bf16_f32 v42, v70, v71
	v_add_u32_e32 v44, 0xffffff00, v44
	v_add_u32_e32 v38, 0xffffff00, v38
	ds_write_b64 v44, v[42:43]
	ds_write_b64 v38, v[40:41]

.LBB0_8:
	s_andn2_b64 vcc, exec, s[8:9]
	v_lshrrev_b32_e32 v45, 5, v131
	v_lshrrev_b32_e32 v44, 5, v132
	v_lshrrev_b32_e32 v43, 5, v133
	v_lshrrev_b32_e32 v42, 5, v134
	v_lshrrev_b32_e32 v41, 5, v135
	v_lshrrev_b32_e32 v40, 5, v136
	v_lshrrev_b32_e32 v39, 5, v137
	v_lshrrev_b32_e32 v38, 5, v138
	s_cbranch_vccnz .LBB0_10
	v_and_b32_e32 v46, 0x7c, v127
	v_mov_b32_e32 v47, 0x8800
	v_lshl_or_b32 v46, v46, 1, v47
	s_movk_i32 s8, 0x110
	v_mad_u32_u24 v47, v45, s8, v46
	ds_write_b64 v47, v[110:111]
	v_mad_u32_u24 v47, v44, s8, v46
	ds_write_b64 v47, v[112:113]
	v_mad_u32_u24 v47, v43, s8, v46
	ds_write_b64 v47, v[114:115]
	v_mad_u32_u24 v47, v42, s8, v46
	ds_write_b64 v47, v[116:117]
	v_mad_u32_u24 v47, v41, s8, v46
	ds_write_b64 v47, v[118:119]
	v_mad_u32_u24 v47, v40, s8, v46
	ds_write_b64 v47, v[120:121]
	v_mad_u32_u24 v47, v39, s8, v46
	v_mad_u32_u24 v46, v38, s8, v46
	ds_write_b64 v47, v[122:123]
	ds_write_b64 v46, v[124:125]
.LBB0_10:
	v_cvt_pk_bf16_f32 v17, v16, v17
	v_cvt_pk_bf16_f32 v16, v14, v15
	v_and_b32_e32 v15, 0x7c, v127
	s_movk_i32 s8, 0x110
	v_lshlrev_b32_e32 v15, 1, v15
	v_cvt_pk_bf16_f32 v13, v12, v13
	v_cvt_pk_bf16_f32 v12, v10, v11
	v_mad_u32_u24 v10, v45, s8, v15
	v_cvt_pk_bf16_f32 v5, v4, v5
	v_cvt_pk_bf16_f32 v4, v2, v3
	v_mad_u32_u24 v2, v44, s8, v15
	ds_write_b64 v10, v[12:13]
	ds_write_b64 v2, v[4:5]
	v_cvt_pk_bf16_f32 v3, v24, v25
	v_cvt_pk_bf16_f32 v2, v22, v23
	v_mad_u32_u24 v4, v43, s8, v15
	ds_write_b64 v4, v[2:3]
	v_cvt_pk_bf16_f32 v3, v8, v9
	v_cvt_pk_bf16_f32 v2, v6, v7
	v_mad_u32_u24 v4, v42, s8, v15
	ds_write_b64 v4, v[2:3]
	v_cvt_pk_bf16_f32 v3, v32, v33
	v_cvt_pk_bf16_f32 v2, v30, v31
	v_mad_u32_u24 v4, v41, s8, v15
	ds_write_b64 v4, v[2:3]
	v_cvt_pk_bf16_f32 v3, v20, v21
	v_cvt_pk_bf16_f32 v2, v18, v19
	v_mad_u32_u24 v4, v40, s8, v15
	ds_write_b64 v4, v[2:3]
	v_cvt_pk_bf16_f32 v3, v36, v37
	v_cvt_pk_bf16_f32 v2, v34, v35
	v_mad_u32_u24 v4, v39, s8, v15
	ds_write_b64 v4, v[2:3]
	v_cvt_pk_bf16_f32 v3, v28, v29
	v_cvt_pk_bf16_f32 v2, v26, v27
	v_mad_u32_u24 v4, v38, s8, v15
	v_lshrrev_b32_e32 v14, 5, v0
	ds_write_b64 v4, v[2:3]
	v_mul_u32_u24_e32 v14, 0x110, v14
	s_mov_b32 s9, 0x1b400
	s_waitcnt lgkmcnt(0)
	v_mov_b32_e32 v109, 0
	v_add3_u32 v14, v14, v15, s9
	ds_write_b64 v14, v[16:17]
	s_waitcnt lgkmcnt(0)
	s_barrier
	s_andn2_b64 vcc, exec, s[6:7]
	s_mov_b32 s4, 0x3db504f3
	s_cbranch_vccnz .LBB0_14
	v_lshrrev_b32_e32 v18, 2, v126
	v_and_b32_e32 v30, 3, v0
	v_mul_u32_u24_e32 v19, 0x104, v18
	s_movk_i32 s4, 0x1040
	v_mad_u32_u24 v19, v128, s4, v19
	v_lshlrev_b32_e32 v20, 6, v30
	s_mov_b32 s4, 0x11000
	v_add3_u32 v19, v19, v20, s4
	ds_read2_b32 v[20:21], v19 offset1:1
	ds_read2_b32 v[24:25], v19 offset0:2 offset1:3
	ds_read2_b32 v[26:27], v19 offset0:4 offset1:5
	ds_read2_b32 v[28:29], v19 offset0:6 offset1:7
	v_cmp_eq_u32_e32 vcc, 0, v30
	s_waitcnt lgkmcnt(3)
	v_add_f32_e32 v20, 0, v20
	v_add_f32_e32 v20, v20, v21
	s_waitcnt lgkmcnt(2)
	v_add_f32_e32 v20, v20, v24
	v_add_f32_e32 v20, v20, v25
	s_waitcnt lgkmcnt(1)
	v_add_f32_e32 v20, v20, v26
	v_add_f32_e32 v20, v20, v27
	s_waitcnt lgkmcnt(0)
	v_add_f32_e32 v24, v20, v28
	ds_read2_b32 v[20:21], v19 offset0:8 offset1:9
	v_add_f32_e32 v31, v24, v29
	ds_read2_b32 v[24:25], v19 offset0:10 offset1:11
	ds_read2_b32 v[26:27], v19 offset0:12 offset1:13
	ds_read2_b32 v[28:29], v19 offset0:14 offset1:15
	s_waitcnt lgkmcnt(3)
	v_add_f32_e32 v19, v31, v20
	v_add_f32_e32 v19, v19, v21
	s_waitcnt lgkmcnt(2)
	v_add_f32_e32 v19, v19, v24
	v_add_f32_e32 v19, v19, v25
	s_waitcnt lgkmcnt(1)
	v_add_f32_e32 v19, v19, v26
	v_add_f32_e32 v19, v19, v27
	s_waitcnt lgkmcnt(0)
	v_add_f32_e32 v19, v19, v28
	v_add_f32_e32 v19, v19, v29
	s_nop 1
	v_add_f32_dpp v19, v19, v19 quad_perm:[1,0,3,2] row_mask:0xf bank_mask:0xf bound_ctrl:1
	s_nop 1
	v_mov_b32_dpp v109, v19 quad_perm:[2,3,0,1] row_mask:0xf bank_mask:0xf
	s_and_saveexec_b64 s[4:5], vcc
	s_cbranch_execz .LBB0_13
	v_lshlrev_b32_e32 v20, 2, v128
	v_lshlrev_b32_e32 v18, 5, v18
	s_mov_b32 s9, 0x1d600
	v_or3_b32 v18, v20, v18, s9
	v_add_f32_e32 v19, v19, v109
	ds_write_b32 v18, v19

.LBB0_28:
	s_waitcnt vmcnt(4)
	v_mov_b32_e32 v44, 0
	v_cmp_ne_u32_e64 s[46:47], 0, v157
	v_cmp_ne_u32_e64 s[48:49], 0, v156
	v_cmp_ne_u32_e64 s[50:51], 0, v155
	v_cmp_ne_u32_e64 s[52:53], 0, v154
	v_addc_co_u32_e64 v44, s[54:55], v44, v44, s[46:47]
	v_addc_co_u32_e64 v44, s[54:55], v44, v44, s[48:49]
	v_addc_co_u32_e64 v44, s[54:55], v44, v44, s[50:51]
	v_addc_co_u32_e64 v44, s[54:55], v44, v44, s[52:53]
	v_cmp_ne_u32_e64 s[46:47], 0, v153
	v_cmp_ne_u32_e64 s[48:49], 0, v152
	v_cmp_ne_u32_e64 s[50:51], 0, v151
	v_cmp_ne_u32_e64 s[52:53], 0, v150
	v_addc_co_u32_e64 v44, s[54:55], v44, v44, s[46:47]
	v_addc_co_u32_e64 v44, s[54:55], v44, v44, s[48:49]
	v_addc_co_u32_e64 v44, s[54:55], v44, v44, s[50:51]
	v_addc_co_u32_e64 v44, s[54:55], v44, v44, s[52:53]
	v_cmp_ne_u32_e64 s[46:47], 0, v149
	v_cmp_ne_u32_e64 s[48:49], 0, v148
	v_cmp_ne_u32_e64 s[50:51], 0, v147
	v_cmp_ne_u32_e64 s[52:53], 0, v146
	v_addc_co_u32_e64 v44, s[54:55], v44, v44, s[46:47]
	v_addc_co_u32_e64 v44, s[54:55], v44, v44, s[48:49]
	v_addc_co_u32_e64 v44, s[54:55], v44, v44, s[50:51]
	v_addc_co_u32_e64 v44, s[54:55], v44, v44, s[52:53]
	v_cmp_ne_u32_e64 s[46:47], 0, v145
	v_cmp_ne_u32_e64 s[48:49], 0, v144
	v_cmp_ne_u32_e64 s[50:51], 0, v143
	v_cmp_ne_u32_e64 s[52:53], 0, v142
	v_addc_co_u32_e64 v44, s[54:55], v44, v44, s[46:47]
	v_addc_co_u32_e64 v44, s[54:55], v44, v44, s[48:49]
	v_addc_co_u32_e64 v44, s[54:55], v44, v44, s[50:51]
	v_addc_co_u32_e64 v44, s[54:55], v44, v44, s[52:53]
	v_lshl_or_b32 v46, s2, 3, v128
	v_lshlrev_b32_e32 v46, 7, v46
	v_lshl_add_u32 v46, v126, 1, v46
	global_store_short v46, v44, s[28:29] sc1
	s_mov_b64 s[8:9], -1
	s_and_b64 vcc, exec, s[6:7]
	s_waitcnt lgkmcnt(0)
	s_barrier
	s_cbranch_vccz .LBB0_34
	v_cmp_gt_u32_e32 vcc, 16, v0
	s_and_saveexec_b64 s[4:5], vcc
	s_cbranch_execz .LBB0_31
	v_or_b32_e32 v18, 0x1d800, v127
	v_add_u32_e32 v19, 0x1d840, v127
	v_add_u32_e32 v20, 0x1d880, v127
	v_add_u32_e32 v21, 0x1d8c0, v127
	v_add_u32_e32 v24, 0x1d900, v127
	v_add_u32_e32 v25, 0x1d940, v127
	v_add_u32_e32 v26, 0x1d980, v127
	v_add_u32_e32 v27, 0x1d9c0, v127
	ds_read_b32 v18, v18
	ds_read_b32 v19, v19
	ds_read_b32 v20, v20
	ds_read_b32 v21, v21
	ds_read_b32 v24, v24
	ds_read_b32 v25, v25
	ds_read_b32 v26, v26
	ds_read_b32 v27, v27
	s_waitcnt lgkmcnt(7)
	v_add_f32_e32 v18, 0, v18
	s_waitcnt lgkmcnt(6)
	v_add_f32_e32 v18, v18, v19
	s_waitcnt lgkmcnt(5)
	v_add_f32_e32 v18, v18, v20
	s_waitcnt lgkmcnt(4)
	v_add_f32_e32 v18, v18, v21
	s_load_dwordx2 s[6:7], s[0:1], 0x60
	s_waitcnt lgkmcnt(0)
	v_add_f32_e32 v18, v18, v24
	v_add_f32_e32 v18, v18, v25
	v_add_f32_e32 v18, v18, v26
	v_add_f32_e32 v20, v18, v27
	v_or_b32_e32 v18, s3, v0
	v_ashrrev_i32_e32 v19, 31, v18
	v_lshl_add_u64 v[18:19], v[18:19], 2, s[6:7]
	global_store_dword v[18:19], v20, off sc1

.LBB0_34:
	s_and_b64 vcc, exec, s[8:9]
	s_cbranch_vccz .LBB0_40
	v_cmp_eq_u32_e32 vcc, 0, v0
	s_and_saveexec_b64 s[6:7], vcc
	s_cbranch_execz .LBB0_37
	v_mov_b32_e32 v18, 0x1d800
	v_mov_b32_e32 v20, 0x1d840
	ds_read_b64 v[18:19], v18
	ds_read_b64 v[20:21], v20
	v_mov_b32_e32 v24, 0x1d880
	v_mov_b32_e32 v26, 0x1d8c0
	ds_read_b64 v[24:25], v24
	ds_read_b64 v[26:27], v26
	s_waitcnt lgkmcnt(0)
	v_max_f32_e32 v18, v18, v18
	v_max_f32_e32 v20, v20, v20
	v_max_f32_e32 v18, v18, v20
	v_add_f32_e32 v19, v19, v21
	v_add_f32_e32 v19, v19, v25
	v_max3_f32 v21, v18, v24, v26
	v_mov_b32_e32 v18, 0x1d900
	v_add_f32_e32 v30, v19, v27
	v_mov_b32_e32 v19, 0x1d940
	v_mov_b32_e32 v20, 0x1d980
	ds_read_b64 v[24:25], v18
	ds_read_b64 v[26:27], v19
	ds_read_b64 v[28:29], v20
	v_mov_b32_e32 v18, 0x1d9c0
	ds_read_b96 v[18:20], v18
	s_mov_b32 s10, 0x3b800000
	s_waitcnt lgkmcnt(2)
	v_max3_f32 v21, v21, v24, v26
	s_waitcnt lgkmcnt(0)
	v_add_f32_e32 v20, v30, v25
	s_mov_b32 s11, 0x3eaab368
	v_max3_f32 v24, v21, v28, v18
	v_mul_f32_e32 v25, v24, v24
	v_add_f32_e32 v20, v20, v27
	v_pk_mul_f32 v[26:27], v[24:25], s[10:11]
	v_add_f32_e32 v20, v20, v29
	v_mov_b32_e32 v28, v26
	v_mul_f32_e32 v21, 0x3ec51eb8, v25
	v_mov_b32_e32 v18, v19
	v_mov_b32_e32 v19, v26
	v_fmac_f32_e32 v28, v24, v27
	v_pk_add_f32 v[18:19], v[20:21], v[18:19]
	s_mov_b32 s3, 0x3a83126f
	v_mul_f32_e32 v20, v18, v28
	s_load_dwordx2 s[8:9], s[0:1], 0x78
	v_cmp_nge_f32_e32 vcc, s3, v20
	v_mul_f32_e32 v18, v18, v19
	s_and_b64 s[10:11], vcc, exec
	v_cmp_nge_f32_e32 vcc, s3, v18
	s_cselect_b32 s12, 3, 2
	s_and_b64 s[10:11], vcc, exec
	s_cselect_b32 s12, s12, 1
	s_ashr_i32 s3, s2, 31
	s_lshl_b64 s[10:11], s[2:3], 2
	s_waitcnt lgkmcnt(0)
	s_add_u32 s8, s8, s10
	s_addc_u32 s9, s9, s11
	v_mov_b32_e32 v18, 0
	v_mov_b32_e32 v19, s12
	global_store_dword v18, v19, s[8:9] sc1

.LBB0_40:
	s_endpgm

	.amdhsa_kernel _Z11prep_kernelPKfS0_S0_S0_S0_S0_S0_S0_S0_PKiPDv8_DF16bS4_PfS5_S5_PiPt
		.amdhsa_group_segment_fixed_size 121344
		.amdhsa_private_segment_fixed_size 0
		.amdhsa_kernarg_size 136
		.amdhsa_user_sgpr_count 2
		.amdhsa_user_sgpr_dispatch_ptr 0
		.amdhsa_user_sgpr_queue_ptr 0
		.amdhsa_user_sgpr_kernarg_segment_ptr 1
		.amdhsa_user_sgpr_dispatch_id 0
		.amdhsa_user_sgpr_kernarg_preload_length 0
		.amdhsa_user_sgpr_kernarg_preload_offset 0
		.amdhsa_user_sgpr_private_segment_size 0
		.amdhsa_uses_dynamic_stack 0
		.amdhsa_enable_private_segment 0
		.amdhsa_system_sgpr_workgroup_id_x 1
		.amdhsa_system_sgpr_workgroup_id_y 0
		.amdhsa_system_sgpr_workgroup_id_z 0
		.amdhsa_system_sgpr_workgroup_info 0
		.amdhsa_system_vgpr_workitem_id 0
		.amdhsa_next_free_vgpr 169
		.amdhsa_next_free_sgpr 96
		.amdhsa_accum_offset 160
		.amdhsa_reserve_vcc 1
		.amdhsa_float_round_mode_32 0
		.amdhsa_float_round_mode_16_64 0
		.amdhsa_float_denorm_mode_32 3
		.amdhsa_float_denorm_mode_16_64 3
		.amdhsa_dx10_clamp 1
		.amdhsa_ieee_mode 1
		.amdhsa_fp16_overflow 0
		.amdhsa_tg_split 0
		.amdhsa_exception_fp_ieee_invalid_op 0
		.amdhsa_exception_fp_denorm_src 0
		.amdhsa_exception_fp_ieee_div_zero 0
		.amdhsa_exception_fp_ieee_overflow 0
		.amdhsa_exception_fp_ieee_underflow 0
		.amdhsa_exception_fp_ieee_inexact 0
		.amdhsa_exception_int_div_zero 0
	.end_amdhsa_kernel

amdhsa.kernels:
  - .agpr_count:     0
    .args:
      - .actual_access:  read_only
        .address_space:  global
        .offset:         0
        .size:           8
        .value_kind:     global_buffer
      - .actual_access:  read_only
        .address_space:  global
        .offset:         8
        .size:           8
        .value_kind:     global_buffer
      - .actual_access:  read_only
        .address_space:  global
        .offset:         16
        .size:           8
        .value_kind:     global_buffer
      - .actual_access:  read_only
        .address_space:  global
        .offset:         24
        .size:           8
        .value_kind:     global_buffer
      - .actual_access:  read_only
        .address_space:  global
        .offset:         32
        .size:           8
        .value_kind:     global_buffer
      - .actual_access:  read_only
        .address_space:  global
        .offset:         40
        .size:           8
        .value_kind:     global_buffer
      - .actual_access:  read_only
        .address_space:  global
        .offset:         48
        .size:           8
        .value_kind:     global_buffer
      - .actual_access:  read_only
        .address_space:  global
        .offset:         56
        .size:           8
        .value_kind:     global_buffer
      - .actual_access:  read_only
        .address_space:  global
        .offset:         64
        .size:           8
        .value_kind:     global_buffer
      - .actual_access:  read_only
        .address_space:  global
        .offset:         72
        .size:           8
        .value_kind:     global_buffer
      - .actual_access:  write_only
        .address_space:  global
        .offset:         80
        .size:           8
        .value_kind:     global_buffer
      - .actual_access:  write_only
        .address_space:  global
        .offset:         88
        .size:           8
        .value_kind:     global_buffer
      - .actual_access:  write_only
        .address_space:  global
        .offset:         96
        .size:           8
        .value_kind:     global_buffer
      - .actual_access:  write_only
        .address_space:  global
        .offset:         104
        .size:           8
        .value_kind:     global_buffer
      - .actual_access:  write_only
        .address_space:  global
        .offset:         112
        .size:           8
        .value_kind:     global_buffer
      - .actual_access:  write_only
        .address_space:  global
        .offset:         120
        .size:           8
        .value_kind:     global_buffer
      - .actual_access:  write_only
        .address_space:  global
        .offset:         128
        .size:           8
        .value_kind:     global_buffer
    .group_segment_fixed_size: 121344
    .kernarg_segment_align: 8
    .kernarg_segment_size: 136
    .language:       OpenCL C
    .language_version:
      - 2
      - 0
    .max_flat_workgroup_size: 512
    .name:           _Z11prep_kernelPKfS0_S0_S0_S0_S0_S0_S0_S0_PKiPDv8_DF16bS4_PfS5_S5_PiPt
    .private_segment_fixed_size: 0
    .sgpr_count:     31
    .sgpr_spill_count: 0
    .symbol:         _Z11prep_kernelPKfS0_S0_S0_S0_S0_S0_S0_S0_PKiPDv8_DF16bS4_PfS5_S5_PiPt.kd
    .uniform_work_group_size: 1
    .uses_dynamic_stack: false
    .vgpr_count:     160
    .vgpr_spill_count: 0
    .wavefront_size: 64
  - .agpr_count:     0
    .args:
      - .actual_access:  read_only
        .address_space:  global
        .offset:         0
        .size:           8
        .value_kind:     global_buffer
      - .actual_access:  read_only
        .address_space:  global
        .offset:         8
        .size:           8
        .value_kind:     global_buffer
      - .actual_access:  read_only
        .address_space:  global
        .offset:         16
        .size:           8
        .value_kind:     global_buffer
      - .actual_access:  read_only
        .address_space:  global
        .offset:         24
        .size:           8
        .value_kind:     global_buffer
      - .actual_access:  read_only
        .address_space:  global
        .offset:         32
        .size:           8
        .value_kind:     global_buffer
      - .actual_access:  read_only
        .address_space:  global
        .offset:         40
        .size:           8
        .value_kind:     global_buffer
      - .actual_access:  read_only
        .address_space:  global
        .offset:         48
        .size:           8
        .value_kind:     global_buffer
      - .actual_access:  read_only
        .address_space:  global
        .offset:         56
        .size:           8
        .value_kind:     global_buffer
      - .actual_access:  read_only
        .address_space:  global
        .offset:         64
        .size:           8
        .value_kind:     global_buffer
      - .actual_access:  write_only
        .address_space:  global
        .offset:         72
        .size:           8
        .value_kind:     global_buffer
    .group_segment_fixed_size: 70400
    .kernarg_segment_align: 8
    .kernarg_segment_size: 80
    .language:       OpenCL C
    .language_version:
      - 2
      - 0
    .max_flat_workgroup_size: 512
    .name:           _Z11main_kernelPKDv8_DF16bS1_PKfS3_S3_PKiPKtS3_S3_Pf
    .private_segment_fixed_size: 0
    .sgpr_count:     54
    .sgpr_spill_count: 0
    .symbol:         _Z11main_kernelPKDv8_DF16bS1_PKfS3_S3_PKiPKtS3_S3_Pf.kd
    .uniform_work_group_size: 1
    .uses_dynamic_stack: false
    .vgpr_count:     204
    .vgpr_spill_count: 0
    .wavefront_size: 64
